# sel block loop: per-block SALU trimmed (3-bit DMA mask, redundant block-present test dropped, scalar diag flag without the VGPR round trip)
# speedup vs baseline: 1.0330x; 1.0064x over previous
; #define RING_BARRIER() do { asm volatile("s_waitcnt lgkmcnt(0)" ::: "memory"); __builtin_amdgcn_s_barrier(); asm volatile("" ::: "memory"); } while (0)
; template <bool DUMMY> __device__ __forceinline__ void sel_phase(Frame& F) {
;     ...
;         for (int p = 0; p < npair; ++p) {
;             u32x2 dnx = {0xffffffffu, 0u}; if (p + 1 < npair) dnx = PD[(p + 1) * 8 + F.wave];
;             asm volatile("s_waitcnt vmcnt(0)" ::: "memory"); RING_BARRIER();
;             const unsigned nj = (unsigned)__builtin_amdgcn_readfirstlane((int)dnx.x), nb = (unsigned)__builtin_amdgcn_readfirstlane((int)dnx.y);
;             if (p + 1 < npair && !(DUMMY && MK_EXP == 2)) { SEL_DMA3(nj, F.lds + ((p + 1) & 1) * 3 * SLOTS); }
.LBB0_1787:
	s_waitcnt vmcnt(0)
	s_waitcnt lgkmcnt(0)
	s_barrier
	s_waitcnt lgkmcnt(0)
	v_readfirstlane_b32 s60, v84
	s_andn2_b64 vcc, exec, s[12:13]
	v_readfirstlane_b32 s61, v85
	s_cbranch_vccnz .LBB0_1796
	s_bitcmp1_b32 s76, 0
	s_cselect_b32 s98, 0xe400, 0
	s_add_i32 s98, s85, s98
	s_lshr_b32 s99, s60, 23
	s_and_b32 s99, s99, 6
	s_or_b32 s99, s99, 1

; #define RING_BARRIER() do { asm volatile("s_waitcnt lgkmcnt(0)" ::: "memory"); __builtin_amdgcn_s_barrier(); asm volatile("" ::: "memory"); } while (0)
; template <bool DUMMY> __device__ __forceinline__ void sel_phase(Frame& F) {
;     ...
;         SEL_DMA3(cj, F.lds);
;         for (int p = 0; p < npair; ++p) {
;             u32x2 dnx = {0xffffffffu, 0u}; if (p + 1 < npair) dnx = PD[(p + 1) * 8 + F.wave];
;             asm volatile("s_waitcnt vmcnt(0)" ::: "memory"); RING_BARRIER();
;             const unsigned nj = (unsigned)__builtin_amdgcn_readfirstlane((int)dnx.x), nb = (unsigned)__builtin_amdgcn_readfirstlane((int)dnx.y);
;             if (p + 1 < npair && !(DUMMY && MK_EXP == 2)) { SEL_DMA3(nj, F.lds + ((p + 1) & 1) * 3 * SLOTS); }
.LBB0_1799:
	s_bitcmp1_b32 s99, s37
	s_cbranch_scc0 .Lsel_nodma

; #define LAS __attribute__((address_space(3)))
; __device__ __forceinline__ unsigned lds_addr(const LAS void* p) { return (unsigned)(size_t)p; }
; template <bool DUMMY> __device__ __forceinline__ void sel_phase(Frame& F) {
;     ...
;             for (int h = 0; h < 3; ++h) {
;                 if (h > 0 && ((cj >> (23 + h)) & 1u) == 0u) continue;
;                 const int jc = (int)((cj >> (8 * h)) & 0xffu);
;                 LAS unsigned char* sb = F.lds + (((p & 1) * 3) + h) * SLOTS;
;                 unsigned byte = (cb >> (8 * h)) & 0xffu;
;                 if (DUMMY && MK_EXP == 1) byte = 0u;
;                 const unsigned a0 = byte & 0xfu, a1 = byte >> 4;
;                 if (byte == 0u) continue;
;                 const bool selA = ((a0 >> (c >> 2)) & 1u) != 0u, selB = ((a1 >> (c >> 2)) & 1u) != 0u;
;                 const float NINF = -__builtin_inff();
;                 const int kb = jc * 64; const bool diag = (jc == cur); f32x4 s0[4], s1[4];
;                 const float bA = selA ? 0.f : NINF, bB = selB ? 0.f : NINF;
;                 if (a0 != 0u) {
;                     const float rf = sm8_ref(g0);
;                     VT8Frag vf; qk8_tile_c(s0, g0, lds_addr(sb) + (unsigned)klane, bA + (5.f - rf)); pv8_issue(vf, lds_addr(sb + K8TB) + (unsigned)vtlane);
;                     if (diag) mask_scores(s0, tokA, 0x40000000u, kb, kq);
.Lsel_nodma:
	s_lshr_b32 s45, s67, s36
	s_and_b32 s97, s45, 0xff
	s_cmp_eq_u32 s97, 0
	s_cbranch_scc1 .LBB0_1798
	s_lshr_b32 s12, s66, s36
	s_and_b32 s12, s12, 0xff
	s_lshl_b32 s44, s12, 6
	s_cmp_eq_u32 s12, s58
	s_cselect_b64 s[12:13], 0, -1
	s_and_b32 vcc_lo, s45, 15
	s_cbranch_scc0 .LBB0_1809
	ds_read_b128 v[84:87], v208 offset:0
	ds_read_b128 v[88:91], v208 offset:16
	ds_read_b128 v[92:95], v208 offset:0x900
	ds_read_b128 v[96:99], v208 offset:0x910
	ds_read_b128 v[118:121], v208 offset:0x1200
	ds_read_b128 v[122:125], v208 offset:0x1210
	ds_read_b128 v[126:129], v208 offset:0x1b00
	ds_read_b128 v[130:133], v208 offset:0x1b10
	v_and_b32_e32 v18, s45, v154
	v_cmp_eq_u32_e32 vcc, 0, v18
	s_nop 1
	v_cndmask_b32_e32 v18, 0, v181, vcc
	v_cmp_ngt_f32_e32 vcc, s90, v19
	s_nop 1
	v_cndmask_b32_e32 v116, 0, v19, vcc
	v_sub_f32_e32 v114, 0x40a00000, v116
	v_add_f32_e32 v210, v114, v18
	v_mov_b32_e32 v211, v210
	v_mov_b32_e32 v212, v210
	v_mov_b32_e32 v213, v210
	s_waitcnt lgkmcnt(6)
	s_nop 1
	v_mfma_scale_f32_16x16x128_f8f6f4 v[84:87], v[84:91], v[0:7], v[210:213], v178, v177 op_sel_hi:[0,0,0]
	ds_read_b64 v[148:149], v207 offset:0
	ds_read_b64 v[146:147], v207 offset:32
	ds_read_b64 v[144:145], v207 offset:0x500
	ds_read_b64 v[142:143], v207 offset:0x520
	ds_read_b64 v[140:141], v207 offset:0xa00
	ds_read_b64 v[136:137], v207 offset:0xa20
	ds_read_b64 v[138:139], v207 offset:0xf00
	ds_read_b64 v[134:135], v207 offset:0xf20
	s_waitcnt lgkmcnt(12)
	v_mfma_scale_f32_16x16x128_f8f6f4 v[88:91], v[92:99], v[0:7], v[210:213], v178, v177 op_sel_hi:[0,0,0]
	s_waitcnt lgkmcnt(10)
	v_mfma_scale_f32_16x16x128_f8f6f4 v[92:95], v[118:125], v[0:7], v[210:213], v178, v177 op_sel_hi:[0,0,0]
	s_waitcnt lgkmcnt(8)
	v_mfma_scale_f32_16x16x128_f8f6f4 v[96:99], v[126:133], v[0:7], v[210:213], v178, v177 op_sel_hi:[0,0,0]
	ds_read_b64 v[132:133], v207 offset:0x1400
	ds_read_b64 v[130:131], v207 offset:0x1420
	ds_read_b64 v[128:129], v207 offset:0x1900
	ds_read_b64 v[126:127], v207 offset:0x1920
	ds_read_b64 v[124:125], v207 offset:0x1e00
	ds_read_b64 v[120:121], v207 offset:0x1e20
	ds_read_b64 v[118:119], v207 offset:0x2300
	ds_read_b64 v[122:123], v207 offset:0x2320
	s_and_b64 vcc, exec, s[12:13]
	s_cbranch_vccnz .LBB0_1806
	v_add_u32_e32 v18, s44, v155
	v_sub_u32_e32 v114, s55, v18
	v_cmp_gt_u32_e32 vcc, 2.0, v114
	v_sub_u32_e32 v114, v18, v16
	s_nop 2
	v_cndmask_b32_e32 v84, v181, v84, vcc
	v_cmp_lt_u32_e32 vcc, s91, v114
	v_sub_u32_e32 v114, v184, v18
	s_nop 0
	v_cndmask_b32_e32 v85, v181, v85, vcc
	v_cmp_gt_u32_e32 vcc, 2.0, v114
	v_sub_u32_e32 v114, v185, v18
	s_nop 0
	v_cndmask_b32_e32 v86, v181, v86, vcc
	v_cmp_gt_u32_e32 vcc, 2.0, v114
	v_sub_u32_e32 v114, s68, v18
	s_nop 0
	v_cndmask_b32_e32 v87, v181, v87, vcc
	v_cmp_gt_u32_e32 vcc, 2.0, v114
	v_sub_u32_e32 v114, v186, v18
	s_nop 0
	v_cndmask_b32_e32 v88, v181, v88, vcc
	v_cmp_gt_u32_e32 vcc, 2.0, v114
	v_sub_u32_e32 v114, v187, v18
	s_nop 0
	v_cndmask_b32_e32 v89, v181, v89, vcc
	v_cmp_gt_u32_e32 vcc, 2.0, v114
	v_sub_u32_e32 v114, v188, v18
	s_nop 0
	v_cndmask_b32_e32 v90, v181, v90, vcc
	v_cmp_gt_u32_e32 vcc, 2.0, v114
	v_sub_u32_e32 v114, s69, v18
	s_nop 0
	v_cndmask_b32_e32 v91, v181, v91, vcc
	v_cmp_gt_u32_e32 vcc, 2.0, v114
	v_sub_u32_e32 v114, v189, v18
	s_nop 0
	v_cndmask_b32_e32 v92, v181, v92, vcc
	v_cmp_gt_u32_e32 vcc, 2.0, v114
	v_sub_u32_e32 v114, v190, v18
	s_nop 0
	v_cndmask_b32_e32 v93, v181, v93, vcc
	v_cmp_gt_u32_e32 vcc, 2.0, v114
	v_sub_u32_e32 v114, v191, v18
	s_nop 0
	v_cndmask_b32_e32 v94, v181, v94, vcc
	v_cmp_gt_u32_e32 vcc, 2.0, v114
	v_sub_u32_e32 v114, s70, v18
	s_nop 0
	v_cndmask_b32_e32 v95, v181, v95, vcc
	v_cmp_gt_u32_e32 vcc, 2.0, v114
	v_sub_u32_e32 v114, v192, v18
	s_nop 0
	v_cndmask_b32_e32 v96, v181, v96, vcc
	v_cmp_gt_u32_e32 vcc, 2.0, v114
	v_sub_u32_e32 v114, v193, v18
	v_sub_u32_e32 v18, v194, v18
	v_cndmask_b32_e32 v97, v181, v97, vcc
	v_cmp_gt_u32_e32 vcc, 2.0, v114
	s_nop 1
	v_cndmask_b32_e32 v98, v181, v98, vcc
	v_cmp_gt_u32_e32 vcc, 2.0, v18
	s_nop 1
	v_cndmask_b32_e32 v99, v181, v99, vcc
